# scan priorities: waves 0-3 prio 1, waves 4-7 prio 2, loader waves prio 0
# speedup vs baseline: 1.0111x; 1.0111x over previous
_Z7k_gemm1PKfS0_PKDv4_jPKiPiS6_P15HIP_vector_typeIiLj2EEPDF16_S0_S6_S9_:
	v_lshrrev_b32_e32 v142, 6, v0
	s_mov_b32 s10, s2
	v_readfirstlane_b32 s90, v0
	s_nop 0
	s_cmp_ge_u32 s90, 0x200
	s_cbranch_scc1 .Lg1_prio_done
	s_setprio 1
	s_cmp_lt_u32 s90, 0x100
	s_cbranch_scc1 .Lg1_prio_done
	s_setprio 2
